# v17: P7 weight (B) tile stage loads issued at the start of the SP2 load segment again (one more interval of HBM latency tolerance), activation tile loads stay in the MFMA block (m1)
# speedup vs baseline: 1.0246x; 1.0108x over previous
.Lp7vg_mmjoin_a:
	s_barrier
	s_add_u32 s2, s44, 0x1000
	s_addc_u32 s3, s45, 0
	s_mov_b32 m0, s19
	v_lshl_add_u64 v[68:69], s[44:45], 0, v[214:215]
	global_load_lds_dwordx4 v[68:69], off
	v_lshl_add_u64 v[68:69], s[44:45], 0, v[218:219]
	s_mov_b32 m0, s33
	s_nop 0
	global_load_lds_dwordx4 v[68:69], off
	v_lshl_add_u64 v[68:69], s[2:3], 0, v[214:215]
	s_mov_b32 m0, s37
	v_lshl_add_u64 v[224:225], s[4:5], 0, v[216:217]
	global_load_lds_dwordx4 v[68:69], off
	v_lshl_add_u64 v[68:69], s[2:3], 0, v[218:219]
	s_mov_b32 m0, s39
	v_cndmask_b32_e64 v66, 0, 1, s[40:41]
	global_load_lds_dwordx4 v[68:69], off
	s_andn2_b64 vcc, exec, s[40:41]
	s_cbranch_vccnz .Lhalfskip_p7a
	ds_read_b128 v[58:61], v236 offset:16384
	ds_read_b128 v[62:65], v236 offset:17408
	ds_read_b128 v[50:53], v236 offset:18432
	ds_read_b128 v[54:57], v236 offset:19456
	ds_read_b128 v[42:45], v236 offset:20480
	ds_read_b128 v[46:49], v236 offset:21504
	ds_read_b128 v[34:37], v236 offset:22528
	ds_read_b128 v[38:41], v236 offset:23552
.Lhalfskip_p7a:
	s_cmp_eq_u32 s100, 3
	s_cbranch_scc1 .Lp7dma_w5_a
	s_cmp_eq_u32 s100, 2
	s_cbranch_scc1 .Lp7dma_wk2_a
	s_waitcnt vmcnt(6)
	s_branch .Lp7dma_wd_a
.Lp7dma_wk2_a:
	s_waitcnt vmcnt(8)
	s_branch .Lp7dma_wd_a
.Lp7dma_w5_a:
	s_waitcnt vmcnt(9)
.Lp7dma_wd_a:
	s_waitcnt lgkmcnt(0)
	s_barrier
	s_cbranch_vccnz .Lp7dma_skip_b
	s_setprio 1
	s_waitcnt lgkmcnt(0)
	v_mfma_scale_f32_16x16x128_f8f6f4 v[138:141], v[26:33], v[58:65], v[138:141], v226, v226 op_sel_hi:[0,0,0]
	v_mfma_scale_f32_16x16x128_f8f6f4 v[134:137], v[18:25], v[58:65], v[134:137], v226, v226 op_sel_hi:[0,0,0]
	v_mfma_scale_f32_16x16x128_f8f6f4 v[122:125], v[26:33], v[50:57], v[122:125], v226, v226 op_sel_hi:[0,0,0]
	v_mfma_scale_f32_16x16x128_f8f6f4 v[118:121], v[18:25], v[50:57], v[118:121], v226, v226 op_sel_hi:[0,0,0]
	v_mfma_scale_f32_16x16x128_f8f6f4 v[106:109], v[26:33], v[42:49], v[106:109], v226, v226 op_sel_hi:[0,0,0]
	v_mfma_scale_f32_16x16x128_f8f6f4 v[102:105], v[18:25], v[42:49], v[102:105], v226, v226 op_sel_hi:[0,0,0]
	v_mfma_scale_f32_16x16x128_f8f6f4 v[90:93], v[26:33], v[34:41], v[90:93], v226, v226 op_sel_hi:[0,0,0]
	v_mfma_scale_f32_16x16x128_f8f6f4 v[86:89], v[18:25], v[34:41], v[86:89], v226, v226 op_sel_hi:[0,0,0]
	s_setprio 0
	s_setprio 1
	v_mfma_scale_f32_16x16x128_f8f6f4 v[130:133], v[10:17], v[58:65], v[130:133], v226, v226 op_sel_hi:[0,0,0]
	v_mfma_scale_f32_16x16x128_f8f6f4 v[126:129], v[2:9], v[58:65], v[126:129], v226, v226 op_sel_hi:[0,0,0]
	v_mfma_scale_f32_16x16x128_f8f6f4 v[114:117], v[10:17], v[50:57], v[114:117], v226, v226 op_sel_hi:[0,0,0]
	v_lshl_add_u64 v[68:69], s[4:5], 0, v[212:213]
	s_mov_b32 m0, s15
	v_cmp_ne_u32_e64 s[2:3], 1, v66
	global_load_lds_dwordx4 v[68:69], off
	v_mfma_scale_f32_16x16x128_f8f6f4 v[110:113], v[2:9], v[50:57], v[110:113], v226, v226 op_sel_hi:[0,0,0]
	v_mfma_scale_f32_16x16x128_f8f6f4 v[98:101], v[10:17], v[42:49], v[98:101], v226, v226 op_sel_hi:[0,0,0]
	s_mov_b32 m0, s49
	s_nop 0
	global_load_lds_dwordx4 v[224:225], off
	v_mfma_scale_f32_16x16x128_f8f6f4 v[94:97], v[2:9], v[42:49], v[94:97], v226, v226 op_sel_hi:[0,0,0]
	v_mfma_scale_f32_16x16x128_f8f6f4 v[82:85], v[10:17], v[34:41], v[82:85], v226, v226 op_sel_hi:[0,0,0]
	v_mfma_scale_f32_16x16x128_f8f6f4 v[78:81], v[2:9], v[34:41], v[78:81], v226, v226 op_sel_hi:[0,0,0]
	s_setprio 0

.Lp7vg_mmjoin_b:
	s_barrier
	v_lshl_add_u64 v[240:241], s[46:47], 0, v[214:215]
	s_add_i32 m0, s15, 0x18000
	s_nop 0
	global_load_lds_dwordx4 v[240:241], off
	s_add_i32 m0, s15, 0x1a000
	v_lshl_add_u64 v[240:241], s[46:47], 0, v[218:219]
	global_load_lds_dwordx4 v[240:241], off
	s_add_u32 s44, s44, 0x85000
	s_addc_u32 s45, s45, 0
	v_lshl_add_u64 v[240:241], s[44:45], 0, v[214:215]
	s_add_i32 m0, s15, 0x1c000
	v_lshl_add_u64 v[68:69], v[68:69], 0, s[10:11]
	global_load_lds_dwordx4 v[240:241], off
	v_lshl_add_u64 v[240:241], s[44:45], 0, v[218:219]
	s_add_i32 m0, s15, 0x1e000
	s_nop 0
	global_load_lds_dwordx4 v[240:241], off
	s_and_b64 vcc, exec, s[2:3]
	s_cbranch_vccnz .Lhalfskip_p7b
	ds_read_b128 v[58:61], v236 offset:49152
	ds_read_b128 v[62:65], v236 offset:50176
	ds_read_b128 v[50:53], v236 offset:51200
	ds_read_b128 v[54:57], v236 offset:52224
	ds_read_b128 v[42:45], v236 offset:53248
	ds_read_b128 v[46:49], v236 offset:54272
	ds_read_b128 v[34:37], v236 offset:55296
	ds_read_b128 v[38:41], v236 offset:56320

.Lp7dma_wd_b:
	s_waitcnt lgkmcnt(0)
	s_barrier
	s_cbranch_vccnz .Lp7dma_skip_d
	s_setprio 1
	s_waitcnt lgkmcnt(0)
	v_mfma_scale_f32_16x16x128_f8f6f4 v[138:141], v[26:33], v[58:65], v[138:141], v226, v226 op_sel_hi:[0,0,0]
	v_mfma_scale_f32_16x16x128_f8f6f4 v[134:137], v[18:25], v[58:65], v[134:137], v226, v226 op_sel_hi:[0,0,0]
	v_mfma_scale_f32_16x16x128_f8f6f4 v[122:125], v[26:33], v[50:57], v[122:125], v226, v226 op_sel_hi:[0,0,0]
	v_mfma_scale_f32_16x16x128_f8f6f4 v[118:121], v[18:25], v[50:57], v[118:121], v226, v226 op_sel_hi:[0,0,0]
	v_mfma_scale_f32_16x16x128_f8f6f4 v[106:109], v[26:33], v[42:49], v[106:109], v226, v226 op_sel_hi:[0,0,0]
	v_mfma_scale_f32_16x16x128_f8f6f4 v[102:105], v[18:25], v[42:49], v[102:105], v226, v226 op_sel_hi:[0,0,0]
	v_mfma_scale_f32_16x16x128_f8f6f4 v[90:93], v[26:33], v[34:41], v[90:93], v226, v226 op_sel_hi:[0,0,0]
	v_mfma_scale_f32_16x16x128_f8f6f4 v[86:89], v[18:25], v[34:41], v[86:89], v226, v226 op_sel_hi:[0,0,0]
	s_setprio 0
	s_setprio 1
	v_mfma_scale_f32_16x16x128_f8f6f4 v[130:133], v[10:17], v[58:65], v[130:133], v226, v226 op_sel_hi:[0,0,0]
	v_mfma_scale_f32_16x16x128_f8f6f4 v[126:129], v[2:9], v[58:65], v[126:129], v226, v226 op_sel_hi:[0,0,0]
	v_mfma_scale_f32_16x16x128_f8f6f4 v[114:117], v[10:17], v[50:57], v[114:117], v226, v226 op_sel_hi:[0,0,0]
	s_mov_b32 m0, s54
	s_nop 0
	global_load_lds_dwordx4 v[68:69], off
	v_mfma_scale_f32_16x16x128_f8f6f4 v[110:113], v[2:9], v[50:57], v[110:113], v226, v226 op_sel_hi:[0,0,0]
	v_mfma_scale_f32_16x16x128_f8f6f4 v[98:101], v[10:17], v[42:49], v[98:101], v226, v226 op_sel_hi:[0,0,0]
	v_lshl_add_u64 v[68:69], v[224:225], 0, s[10:11]
	s_mov_b32 m0, s55
	s_nop 0
	global_load_lds_dwordx4 v[68:69], off
	v_mfma_scale_f32_16x16x128_f8f6f4 v[94:97], v[2:9], v[42:49], v[94:97], v226, v226 op_sel_hi:[0,0,0]
	v_mfma_scale_f32_16x16x128_f8f6f4 v[82:85], v[10:17], v[34:41], v[82:85], v226, v226 op_sel_hi:[0,0,0]
	v_mfma_scale_f32_16x16x128_f8f6f4 v[78:81], v[2:9], v[34:41], v[78:81], v226, v226 op_sel_hi:[0,0,0]
	s_setprio 0
	s_branch .LBB0_781
.Lp7dma_skip_b:
	v_lshl_add_u64 v[68:69], s[4:5], 0, v[212:213]
	s_mov_b32 m0, s15
	v_cmp_ne_u32_e64 s[2:3], 1, v66
	global_load_lds_dwordx4 v[68:69], off
	s_mov_b32 m0, s49
	s_nop 0
	global_load_lds_dwordx4 v[224:225], off
	s_branch .LBB0_790
.Lp7dma_skip_d:
	s_mov_b32 m0, s54
	s_nop 0
	global_load_lds_dwordx4 v[68:69], off
	v_lshl_add_u64 v[68:69], v[224:225], 0, s[10:11]
	s_mov_b32 m0, s55
	s_nop 0
	global_load_lds_dwordx4 v[68:69], off
	s_branch .LBB0_781
